# strategy 7.2 (wait at first consumer) in the dense attention unit prologue: the full drain before the first QK MFMA becomes per-fragment counted waits (the 4th K/V tile request stays in flight)
# baseline (speedup 1.0000x reference)
.LBB0_728:
	v_lshl_add_u64 v[50:51], s[4:5], 1, v[202:203]
	s_mov_b32 s13, m0
	s_mov_b32 m0, s34
	s_nop 0
	global_load_lds_dwordx4 v[50:51], off
	s_mov_b32 m0, s13
	v_lshl_add_u64 v[48:49], s[20:21], 1, v[204:205]
	s_mov_b32 s13, m0
	s_mov_b32 m0, s35
	s_nop 0
	global_load_lds_dwordx4 v[48:49], off
	s_mov_b32 m0, s13
	s_cmp_lg_u32 0, -1
	s_mov_b64 s[24:25], 0x48000
	s_cselect_b32 s13, 0, 0
	v_lshl_add_u64 v[0:1], v[50:51], 0, s[24:25]
	s_add_i32 s13, s13, s12
	s_add_i32 s14, s13, 0x2000
	s_mov_b32 s15, m0
	s_mov_b32 m0, s14
	s_nop 0
	global_load_lds_dwordx4 v[0:1], off
	s_mov_b32 m0, s15
	v_lshl_add_u64 v[0:1], s[22:23], 1, v[206:207]
	s_nop 0
	global_load_dwordx4 v[140:143], v[0:1], off
	global_load_dwordx4 v[132:135], v[0:1], off offset:32
	global_load_dwordx4 v[120:123], v[0:1], off offset:64
	global_load_dwordx4 v[116:119], v[0:1], off offset:96
	v_mov_b32_e32 v15, 0
	s_mov_b64 s[14:15], 0x90000
	v_mov_b32_e32 v14, v15
	v_mov_b32_e32 v0, v15
	v_mov_b32_e32 v1, v15
	v_mov_b32_e32 v2, v15
	v_mov_b32_e32 v3, v15
	v_mov_b32_e32 v4, v15
	v_mov_b32_e32 v5, v15
	v_mov_b32_e32 v6, v15
	v_mov_b32_e32 v7, v15
	v_mov_b32_e32 v8, v15
	v_mov_b32_e32 v9, v15
	v_mov_b32_e32 v10, v15
	v_mov_b32_e32 v11, v15
	v_mov_b32_e32 v12, v15
	v_mov_b32_e32 v13, v15
	s_waitcnt lgkmcnt(0)
	v_mov_b64_e32 v[30:31], v[14:15]
	v_mov_b64_e32 v[28:29], v[12:13]
	v_mov_b64_e32 v[26:27], v[10:11]
	v_mov_b64_e32 v[24:25], v[8:9]
	v_mov_b64_e32 v[22:23], v[6:7]
	v_mov_b64_e32 v[20:21], v[4:5]
	v_mov_b64_e32 v[18:19], v[2:3]
	v_mov_b64_e32 v[16:17], v[0:1]
	v_lshl_add_u64 v[32:33], v[50:51], 0, s[14:15]
	s_add_i32 s14, s13, 0x4000
	s_mov_b32 s15, m0
	s_mov_b32 m0, s14
	s_nop 0
	global_load_lds_dwordx4 v[32:33], off
	s_mov_b32 m0, s15
	s_waitcnt vmcnt(3) lgkmcnt(0)
	s_barrier
	ds_read_b128 v[0:3], v65
	ds_read_b128 v[4:7], v65 offset:512
	s_mov_b64 s[14:15], 0xd8000
	s_add_i32 s13, s13, 0x8000
	s_andn2_b64 vcc, exec, s[2:3]
	s_mov_b64 s[2:3], -1
	s_waitcnt lgkmcnt(0)
	v_mfma_f32_32x32x16_bf16 v[32:47], v[0:3], v[140:143], v[16:31]
	v_mfma_f32_32x32x16_bf16 v[16:31], v[4:7], v[140:143], v[16:31]
	ds_read_b128 v[0:3], v65 offset:2048
	ds_read_b128 v[4:7], v65 offset:2560
	s_waitcnt lgkmcnt(1)
	v_mfma_f32_32x32x16_bf16 v[32:47], v[0:3], v[132:135], v[32:47]
	s_waitcnt lgkmcnt(0)
	v_mfma_f32_32x32x16_bf16 v[16:31], v[4:7], v[132:135], v[16:31]
	ds_read_b128 v[0:3], v65 offset:4096
	ds_read_b128 v[4:7], v65 offset:4608
	s_waitcnt vmcnt(2) lgkmcnt(1)
	v_mfma_f32_32x32x16_bf16 v[32:47], v[0:3], v[120:123], v[32:47]
	s_waitcnt lgkmcnt(0)
	v_mfma_f32_32x32x16_bf16 v[16:31], v[4:7], v[120:123], v[16:31]
	ds_read_b128 v[0:3], v65 offset:6144
	ds_read_b128 v[4:7], v65 offset:6656
	s_waitcnt vmcnt(1) lgkmcnt(1)
	v_mfma_f32_32x32x16_bf16 v[32:47], v[0:3], v[116:119], v[32:47]
	s_waitcnt lgkmcnt(0)
	v_mfma_f32_32x32x16_bf16 v[16:31], v[4:7], v[116:119], v[16:31]
	s_nop 15
	s_nop 7
	s_nop 0
	v_max3_f32 v0, v32, v33, v16
	v_max3_f32 v1, v34, v35, v17
	s_nop 0
	v_max3_f32 v0, v0, v18, v19
	v_max3_f32 v1, v1, v38, v39
	s_nop 0
	v_max3_f32 v0, v0, v36, v37
	v_max3_f32 v1, v1, v22, v23
	s_nop 0
	v_max3_f32 v0, v0, v20, v21
	v_max3_f32 v1, v1, v42, v43
	s_nop 0
	v_max3_f32 v0, v0, v40, v41
	v_max3_f32 v1, v1, v26, v27
	s_nop 0
	v_max3_f32 v0, v0, v24, v25
	v_max3_f32 v1, v1, v46, v47
	s_nop 0
	v_max3_f32 v0, v0, v44, v45
	v_max3_f32 v1, v1, v30, v31
	s_nop 0
	v_max3_f32 v0, v0, v28, v29
	s_nop 0
	v_max_f32_e32 v0, v0, v1
	s_nop 0
	v_mov_b32_e32 v1, v0
	s_nop 1
	v_permlane32_swap_b32_e32 v0, v1
	v_max_f32_e32 v0, v0, v1
	s_nop 0
	v_add_f32_e32 v234, v115, v0
	v_sub_f32_e32 v1, v32, v0
	v_sub_f32_e32 v2, v16, v0
	v_sub_f32_e32 v3, v33, v0
	v_sub_f32_e32 v4, v17, v0
	v_sub_f32_e32 v5, v34, v0
	s_nop 0
	v_xor_b32_e32 v66, 0x80000000, v234
	v_mov_b32_e32 v67, v66
	v_mov_b32_e32 v68, v66
	v_mov_b32_e32 v69, v66
	v_mov_b32_e32 v70, v66
	v_mov_b32_e32 v71, v66
	v_mov_b32_e32 v72, v66
	v_mov_b32_e32 v73, v66
	v_mov_b32_e32 v74, v66
	v_mov_b32_e32 v75, v66
	v_mov_b32_e32 v76, v66
	v_mov_b32_e32 v77, v66
	v_mov_b32_e32 v78, v66
	v_mov_b32_e32 v79, v66
	v_mov_b32_e32 v80, v66
	v_mov_b32_e32 v81, v66
	v_sub_f32_e32 v6, v18, v0
	v_sub_f32_e32 v7, v35, v0
	v_sub_f32_e32 v8, v19, v0
	v_sub_f32_e32 v9, v36, v0
	v_sub_f32_e32 v10, v20, v0
	v_sub_f32_e32 v11, v37, v0
	v_sub_f32_e32 v12, v21, v0
	v_sub_f32_e32 v13, v38, v0
	v_sub_f32_e32 v14, v22, v0
	v_sub_f32_e32 v16, v39, v0
	v_sub_f32_e32 v17, v23, v0
	v_sub_f32_e32 v18, v40, v0
	v_sub_f32_e32 v19, v24, v0
	v_sub_f32_e32 v20, v41, v0
	v_sub_f32_e32 v21, v25, v0
	v_sub_f32_e32 v22, v42, v0
	v_sub_f32_e32 v23, v26, v0
	v_sub_f32_e32 v24, v43, v0
	v_sub_f32_e32 v25, v27, v0
	v_sub_f32_e32 v26, v44, v0
	v_sub_f32_e32 v27, v28, v0
	v_sub_f32_e32 v28, v45, v0
	v_sub_f32_e32 v29, v29, v0
	v_sub_f32_e32 v32, v46, v0
	v_sub_f32_e32 v30, v30, v0
	v_sub_f32_e32 v33, v47, v0
	v_sub_f32_e32 v0, v31, v0
	s_waitcnt vmcnt(0) lgkmcnt(0)
	s_barrier
	v_exp_f32_e32 v98, v1
	v_exp_f32_e32 v97, v0
	v_lshl_add_u64 v[0:1], v[50:51], 0, s[14:15]
	s_mov_b32 s14, m0
	s_mov_b32 m0, s34
	s_nop 0
	global_load_lds_dwordx4 v[0:1], off
	s_mov_b32 m0, s14
	v_lshl_add_u64 v[0:1], v[48:49], 0, s[24:25]
	s_mov_b32 s14, m0
	s_mov_b32 m0, s13
	s_nop 0
	global_load_lds_dwordx4 v[0:1], off
	s_mov_b32 m0, s14
	ds_read_b128 v[176:179], v65 offset:8192
	ds_read_b128 v[172:175], v65 offset:8704
	ds_read_b128 v[168:171], v65 offset:10240
	ds_read_b128 v[164:167], v65 offset:10752
	ds_read_b128 v[160:163], v65 offset:12288
	ds_read_b128 v[156:159], v65 offset:12800
	ds_read_b128 v[152:155], v65 offset:14336
	ds_read_b128 v[148:151], v65 offset:14848
	v_exp_f32_e32 v99, v3
	v_exp_f32_e32 v100, v5
	v_exp_f32_e32 v101, v7
	v_exp_f32_e32 v102, v9
	v_exp_f32_e32 v103, v11
	v_exp_f32_e32 v104, v13
	v_exp_f32_e32 v105, v16
	v_exp_f32_e32 v106, v18
	v_exp_f32_e32 v107, v20
	v_exp_f32_e32 v108, v22
	v_exp_f32_e32 v109, v24
	v_exp_f32_e32 v110, v26
	v_exp_f32_e32 v111, v28
	v_exp_f32_e32 v112, v32
	v_exp_f32_e32 v113, v33
	v_exp_f32_e32 v82, v2
	v_exp_f32_e32 v83, v4
	v_exp_f32_e32 v84, v6
	v_exp_f32_e32 v85, v8
	v_exp_f32_e32 v86, v10
	v_exp_f32_e32 v87, v12
	v_exp_f32_e32 v88, v14
	v_exp_f32_e32 v89, v17
	v_exp_f32_e32 v90, v19
	v_exp_f32_e32 v91, v21
	v_exp_f32_e32 v92, v23
	v_exp_f32_e32 v93, v25
	v_exp_f32_e32 v94, v27
	v_exp_f32_e32 v95, v29
	v_exp_f32_e32 v96, v30
	s_waitcnt vmcnt(2) lgkmcnt(0)
	s_barrier
	s_cbranch_vccnz .LBB0_730
	v_mov_b32_e32 v30, v15
	v_mov_b32_e32 v31, v15
	v_mov_b32_e32 v0, v15
	v_mov_b32_e32 v1, v15
	v_mov_b32_e32 v2, v15
	v_mov_b32_e32 v3, v15
	v_mov_b32_e32 v4, v15
	v_mov_b32_e32 v5, v15
	v_mov_b32_e32 v6, v15
	v_mov_b32_e32 v7, v15
	v_mov_b32_e32 v8, v15
	v_mov_b32_e32 v9, v15
	v_mov_b32_e32 v10, v15
	v_mov_b32_e32 v11, v15
	v_mov_b32_e32 v12, v15
	v_mov_b32_e32 v13, v15
	v_mov_b32_e32 v14, v15
	v_mov_b32_e32 v16, v15
	v_mov_b32_e32 v17, v15
	v_mov_b32_e32 v18, v15
	v_mov_b32_e32 v19, v15
	v_mov_b32_e32 v20, v15
	v_mov_b32_e32 v21, v15
	v_mov_b32_e32 v22, v15
	v_mov_b32_e32 v23, v15
	v_mov_b32_e32 v24, v15
	v_mov_b32_e32 v25, v15
	v_mov_b32_e32 v26, v15
	v_mov_b32_e32 v27, v15
	v_mov_b32_e32 v28, v15
	v_mov_b32_e32 v29, v15
	v_mov_b64_e32 v[62:63], v[30:31]
	s_mov_b64 s[2:3], 0
	v_mov_b64_e32 v[60:61], v[28:29]
	v_mov_b64_e32 v[58:59], v[26:27]
	v_mov_b64_e32 v[56:57], v[24:25]
	v_mov_b64_e32 v[54:55], v[22:23]
	v_mov_b64_e32 v[52:53], v[20:21]
	v_mov_b64_e32 v[50:51], v[18:19]
	v_mov_b64_e32 v[48:49], v[16:17]
	v_mov_b64_e32 v[46:47], v[14:15]
	v_mov_b64_e32 v[44:45], v[12:13]
	v_mov_b64_e32 v[42:43], v[10:11]
	v_mov_b64_e32 v[40:41], v[8:9]
	v_mov_b64_e32 v[38:39], v[6:7]
	v_mov_b64_e32 v[36:37], v[4:5]
	v_mov_b64_e32 v[34:35], v[2:3]
	v_mov_b64_e32 v[32:33], v[0:1]
